# baseline (speedup 1.0000x reference)
_Z11prep_kernelPKfS0_S0_S0_S0_S0_S0_S0_S0_PKiPDv8_DF16bS4_PfS5_S5_PiPt:
	s_load_dwordx4 s[16:19], s[0:1], 0x0
	s_load_dwordx4 s[20:23], s[0:1], 0x10
	s_load_dwordx4 s[24:27], s[0:1], 0x20
	s_load_dwordx4 s[28:31], s[0:1], 0x30
	s_load_dwordx4 s[32:35], s[0:1], 0x40
	s_load_dwordx2 s[36:37], s[0:1], 0x80
	v_and_b32_e32 v126, 63, v0
	v_lshrrev_b32_e32 v128, 6, v0
	v_and_b32_e32 v1, 15, v0
	v_bfe_u32 v24, v0, 4, 2
	v_lshl_or_b32 v107, v128, 4, v1
	v_lshlrev_b32_e32 v106, 2, v107
	v_lshlrev_b32_e32 v127, 2, v0
	v_lshlrev_b32_e32 v25, 1, v107
	v_and_b32_e32 v26, 48, v0
	v_mul_u32_u24_e32 v27, 0x440, v24
	v_lshlrev_b32_e32 v120, 4, v0
	v_lshrrev_b32_e32 v58, 5, v0
	v_mul_u32_u24_e32 v58, 0x110, v58
	v_and_b32_e32 v125, 31, v0
	v_lshl_add_u32 v58, v125, 3, v58
	v_add_u32_e32 v124, 0x1b400, v58
	v_mul_u32_u24_e32 v52, 0x110, v1
	v_add_u32_e32 v52, v52, v26
	v_add_u32_e32 v53, 0x1b400, v52
	v_add_u32_e32 v54, 0x1c500, v52
	v_add_u32_e32 v55, v27, v25
	v_add_u32_e32 v55, 0x1c500, v55
	v_mul_u32_u24_e32 v56, 0x110, v107
	v_add_u32_e32 v56, v56, v26
	v_add_u32_e32 v57, 0x8800, v56
	s_lshl_b32 s12, s2, 4
	s_add_i32 s3, s12, 0xfffff800
	s_cmpk_gt_i32 s2, 0x7f
	s_cselect_b64 s[6:7], -1, 0
	s_mov_b32 s48, 0
	s_mov_b32 s49, -1
	v_lshl_or_b32 v123, s2, 3, v128
	v_lshlrev_b32_e32 v123, 12, v123
	v_lshl_add_u32 v123, v126, 4, v123
	s_waitcnt lgkmcnt(0)
	s_cmpk_lt_i32 s2, 0x80
	s_cselect_b32 s38, s16, s18
	s_cselect_b32 s39, s17, s19
	s_cselect_b32 s40, s20, s24
	s_cselect_b32 s41, s21, s25
	s_cselect_b32 s13, s12, s3
	s_cselect_b32 s44, 0x3db504f3, 1.0
	s_lshl_b32 s13, s13, 9
	s_add_u32 s38, s38, s13
	s_addc_u32 s39, s39, 0
	global_load_dwordx4 v[2:5], v120, s[38:39] nt
	s_and_b64 vcc, exec, s[6:7]
	s_cbranch_vccz .Lp_q
	v_lshlrev_b32_e32 v48, 13, v128
	v_lshl_add_u32 v48, v126, 4, v48
	s_and_b32 s13, s2, 7
	s_lshl_b32 s14, s13, 10
	v_add_u32_e32 v125, s14, v48
	global_load_dwordx4 v[80:83], v125, s[40:41]
	s_add_i32 s13, s2, 1
	s_and_b32 s13, s13, 7
	s_lshl_b32 s14, s13, 10
	v_add_u32_e32 v125, s14, v48
	global_load_dwordx4 v[84:87], v125, s[40:41]
	s_add_i32 s13, s2, 2
	s_and_b32 s13, s13, 7
	s_lshl_b32 s14, s13, 10
	v_add_u32_e32 v125, s14, v48
	global_load_dwordx4 v[88:91], v125, s[40:41]
	s_add_i32 s13, s2, 3
	s_and_b32 s13, s13, 7
	s_lshl_b32 s14, s13, 10
	v_add_u32_e32 v125, s14, v48
	global_load_dwordx4 v[92:95], v125, s[40:41]
	s_add_i32 s13, s2, 4
	s_and_b32 s13, s13, 7
	s_lshl_b32 s14, s13, 10
	v_add_u32_e32 v125, s14, v48
	global_load_dwordx4 v[96:99], v125, s[40:41]
	s_add_i32 s13, s2, 5
	s_and_b32 s13, s13, 7
	s_lshl_b32 s14, s13, 10
	v_add_u32_e32 v125, s14, v48
	global_load_dwordx4 v[100:103], v125, s[40:41]
	s_add_i32 s13, s2, 6
	s_and_b32 s13, s13, 7
	s_lshl_b32 s14, s13, 10
	v_add_u32_e32 v125, s14, v48
	global_load_dwordx4 v[108:111], v125, s[40:41]
	s_add_i32 s13, s2, 7
	s_and_b32 s13, s13, 7
	s_lshl_b32 s14, s13, 10
	v_add_u32_e32 v125, s14, v48
	global_load_dwordx4 v[112:115], v125, s[40:41]
	global_load_dword v129, v106, s[32:33]
	global_load_dword v130, v106, s[30:31]
	v_lshrrev_b32_e32 v49, 5, v126
	v_lshl_add_u32 v49, v128, 4, v49
	v_mul_u32_u24_e32 v49, 0x110, v49
	v_and_b32_e32 v125, 31, v126
	v_lshl_add_u32 v49, v125, 3, v49
	v_cmp_gt_u32_e32 vcc, 32, v126
	v_mov_b32_e32 v198, 0x3db504f3
	v_mov_b32_e32 v125, s22
	v_mov_b32_e32 v104, s26
	v_cndmask_b32_e32 v198, 1.0, v198, vcc
	v_cndmask_b32_e32 v104, v104, v125, vcc
	v_mov_b32_e32 v125, s23
	v_mov_b32_e32 v105, s27
	v_cndmask_b32_e32 v105, v105, v125, vcc
	v_and_b32_e32 v196, 31, v126
	v_lshlrev_b32_e32 v196, 4, v196
	v_mov_b32_e32 v197, 0
	v_lshl_add_u64 v[104:105], v[104:105], 0, v[196:197]
	global_load_dwordx4 v[116:119], v[104:105], off
	v_lshlrev_b32_e32 v121, 14, v128
	v_lshl_add_u32 v121, v126, 4, v121
	s_and_b32 s13, s2, 15
	s_lshl_b32 s14, s13, 10
	s_add_u32 s46, s28, s14
	s_addc_u32 s47, s29, 0
	global_load_dwordx4 v[132:135], v121, s[46:47]
	s_add_i32 s13, s2, 1
	s_and_b32 s13, s13, 15
	s_lshl_b32 s14, s13, 10
	s_add_u32 s46, s28, s14
	s_addc_u32 s47, s29, 0
	global_load_dwordx4 v[136:139], v121, s[46:47]
	s_add_i32 s13, s2, 2
	s_and_b32 s13, s13, 15
	s_lshl_b32 s14, s13, 10
	s_add_u32 s46, s28, s14
	s_addc_u32 s47, s29, 0
	global_load_dwordx4 v[140:143], v121, s[46:47]
	s_add_i32 s13, s2, 3
	s_and_b32 s13, s13, 15
	s_lshl_b32 s14, s13, 10
	s_add_u32 s46, s28, s14
	s_addc_u32 s47, s29, 0
	global_load_dwordx4 v[144:147], v121, s[46:47]
	s_add_i32 s13, s2, 4
	s_and_b32 s13, s13, 15
	s_lshl_b32 s14, s13, 10
	s_add_u32 s46, s28, s14
	s_addc_u32 s47, s29, 0
	global_load_dwordx4 v[148:151], v121, s[46:47]
	s_add_i32 s13, s2, 5
	s_and_b32 s13, s13, 15
	s_lshl_b32 s14, s13, 10
	s_add_u32 s46, s28, s14
	s_addc_u32 s47, s29, 0
	global_load_dwordx4 v[152:155], v121, s[46:47]
	s_add_i32 s13, s2, 6
	s_and_b32 s13, s13, 15
	s_lshl_b32 s14, s13, 10
	s_add_u32 s46, s28, s14
	s_addc_u32 s47, s29, 0
	global_load_dwordx4 v[156:159], v121, s[46:47]
	s_add_i32 s13, s2, 7
	s_and_b32 s13, s13, 15
	s_lshl_b32 s14, s13, 10
	s_add_u32 s46, s28, s14
	s_addc_u32 s47, s29, 0
	global_load_dwordx4 v[160:163], v121, s[46:47]
	s_add_i32 s13, s2, 8
	s_and_b32 s13, s13, 15
	s_lshl_b32 s14, s13, 10
	s_add_u32 s46, s28, s14
	s_addc_u32 s47, s29, 0
	global_load_dwordx4 v[164:167], v121, s[46:47]
	s_add_i32 s13, s2, 9
	s_and_b32 s13, s13, 15
	s_lshl_b32 s14, s13, 10
	s_add_u32 s46, s28, s14
	s_addc_u32 s47, s29, 0
	global_load_dwordx4 v[168:171], v121, s[46:47]
	s_add_i32 s13, s2, 10
	s_and_b32 s13, s13, 15
	s_lshl_b32 s14, s13, 10
	s_add_u32 s46, s28, s14
	s_addc_u32 s47, s29, 0
	global_load_dwordx4 v[172:175], v121, s[46:47]
	s_add_i32 s13, s2, 11
	s_and_b32 s13, s13, 15
	s_lshl_b32 s14, s13, 10
	s_add_u32 s46, s28, s14
	s_addc_u32 s47, s29, 0
	global_load_dwordx4 v[176:179], v121, s[46:47]
	s_add_i32 s13, s2, 12
	s_and_b32 s13, s13, 15
	s_lshl_b32 s14, s13, 10
	s_add_u32 s46, s28, s14
	s_addc_u32 s47, s29, 0
	global_load_dwordx4 v[180:183], v121, s[46:47]
	s_add_i32 s13, s2, 13
	s_and_b32 s13, s13, 15
	s_lshl_b32 s14, s13, 10
	s_add_u32 s46, s28, s14
	s_addc_u32 s47, s29, 0
	global_load_dwordx4 v[184:187], v121, s[46:47]
	s_add_i32 s13, s2, 14
	s_and_b32 s13, s13, 15
	s_lshl_b32 s14, s13, 10
	s_add_u32 s46, s28, s14
	s_addc_u32 s47, s29, 0
	global_load_dwordx4 v[188:191], v121, s[46:47]
	s_add_i32 s13, s2, 15
	s_and_b32 s13, s13, 15
	s_lshl_b32 s14, s13, 10
	s_add_u32 s46, s28, s14
	s_addc_u32 s47, s29, 0
	global_load_dwordx4 v[192:195], v121, s[46:47]
	v_mul_u32_u24_e32 v59, 0x1040, v128
	v_lshl_add_u32 v59, v126, 2, v59
	v_add_u32_e32 v59, 0x11000, v59
	v_mul_u32_u24_e32 v76, 0x1100, v128
	v_lshl_add_u32 v76, v126, 3, v76
	v_add_u32_e32 v76, 0x8700, v76
	v_lshrrev_b32_e32 v77, 2, v126
	v_mul_u32_u24_e32 v77, 0x104, v77
	v_mul_u32_u24_e32 v125, 0x1040, v128
	v_add_u32_e32 v77, v77, v125
	v_and_b32_e32 v125, 3, v126
	v_lshl_add_u32 v77, v125, 6, v77
	v_add_u32_e32 v77, 0x11000, v77
	s_waitcnt vmcnt(27)
	v_cvt_pk_bf16_f32 v12, v2, v3
	v_cvt_pk_bf16_f32 v13, v4, v5
	ds_write_b64 v124, v[12:13]
	s_waitcnt lgkmcnt(0)
	s_barrier
	s_waitcnt vmcnt(26)
	v_cvt_pk_bf16_f32 v6, v80, v81
	v_cvt_pk_bf16_f32 v7, v82, v83
	s_and_b32 s13, s2, 7
	s_mul_i32 s14, s13, 0x220
	v_add_u32_e32 v125, s14, v49
	ds_write_b64 v125, v[6:7]
	s_waitcnt vmcnt(25)
	v_cvt_pk_bf16_f32 v8, v84, v85
	v_cvt_pk_bf16_f32 v9, v86, v87
	s_add_i32 s13, s2, 1
	s_and_b32 s13, s13, 7
	s_mul_i32 s14, s13, 0x220
	v_add_u32_e32 v10, s14, v49
	ds_write_b64 v10, v[8:9]
	s_waitcnt vmcnt(24)
	v_cvt_pk_bf16_f32 v6, v88, v89
	v_cvt_pk_bf16_f32 v7, v90, v91
	s_add_i32 s13, s2, 2
	s_and_b32 s13, s13, 7
	s_mul_i32 s14, s13, 0x220
	v_add_u32_e32 v125, s14, v49
	ds_write_b64 v125, v[6:7]
	s_waitcnt vmcnt(23)
	v_cvt_pk_bf16_f32 v8, v92, v93
	v_cvt_pk_bf16_f32 v9, v94, v95
	s_add_i32 s13, s2, 3
	s_and_b32 s13, s13, 7
	s_mul_i32 s14, s13, 0x220
	v_add_u32_e32 v10, s14, v49
	ds_write_b64 v10, v[8:9]
	s_waitcnt vmcnt(22)
	v_cvt_pk_bf16_f32 v6, v96, v97
	v_cvt_pk_bf16_f32 v7, v98, v99
	s_add_i32 s13, s2, 4
	s_and_b32 s13, s13, 7
	s_mul_i32 s14, s13, 0x220
	v_add_u32_e32 v125, s14, v49
	ds_write_b64 v125, v[6:7]
	s_waitcnt vmcnt(21)
	v_cvt_pk_bf16_f32 v8, v100, v101
	v_cvt_pk_bf16_f32 v9, v102, v103
	s_add_i32 s13, s2, 5
	s_and_b32 s13, s13, 7
	s_mul_i32 s14, s13, 0x220
	v_add_u32_e32 v10, s14, v49
	ds_write_b64 v10, v[8:9]
	s_waitcnt vmcnt(20)
	v_cvt_pk_bf16_f32 v6, v108, v109
	v_cvt_pk_bf16_f32 v7, v110, v111
	s_add_i32 s13, s2, 6
	s_and_b32 s13, s13, 7
	s_mul_i32 s14, s13, 0x220
	v_add_u32_e32 v125, s14, v49
	ds_write_b64 v125, v[6:7]
	s_waitcnt vmcnt(19)
	v_cvt_pk_bf16_f32 v8, v112, v113
	v_cvt_pk_bf16_f32 v9, v114, v115
	s_add_i32 s13, s2, 7
	s_and_b32 s13, s13, 7
	s_mul_i32 s14, s13, 0x220
	v_add_u32_e32 v10, s14, v49
	ds_write_b64 v10, v[8:9]
	ds_read_b128 v[28:31], v53
	ds_read_b128 v[60:63], v56
	ds_read_b128 v[32:35], v53 offset:64
	ds_read_b128 v[64:67], v56 offset:64
	ds_read_b128 v[36:39], v53 offset:128
	ds_read_b128 v[68:71], v56 offset:128
	ds_read_b128 v[40:43], v53 offset:192
	ds_read_b128 v[72:75], v56 offset:192
	s_waitcnt lgkmcnt(6)
	v_mfma_f32_16x16x32_bf16 v[18:21], v[28:31], v[60:63], 0
	s_waitcnt lgkmcnt(4)
	v_mfma_f32_16x16x32_bf16 v[18:21], v[32:35], v[64:67], v[18:21]
	s_waitcnt lgkmcnt(2)
	v_mfma_f32_16x16x32_bf16 v[18:21], v[36:39], v[68:71], v[18:21]
	s_waitcnt lgkmcnt(0)
	v_mfma_f32_16x16x32_bf16 v[18:21], v[40:43], v[72:75], v[18:21]
	s_nop 7
	v_mul_f32_e32 v18, s44, v18
	v_mul_f32_e32 v19, s44, v19
	v_mul_f32_e32 v20, s44, v20
	v_mul_f32_e32 v21, s44, v21
	v_cvt_pk_bf16_f32 v18, v18, v18
	v_cvt_pk_bf16_f32 v19, v19, v19
	v_cvt_pk_bf16_f32 v20, v20, v20
	v_cvt_pk_bf16_f32 v21, v21, v21
	ds_write_b16 v55, v18
	ds_write_b16 v55, v19 offset:272
	ds_write_b16 v55, v20 offset:544
	ds_write_b16 v55, v21 offset:816
	s_waitcnt vmcnt(16)
	v_pk_mul_f32 v[116:117], v[198:199], v[116:117] op_sel_hi:[0,1]
	v_pk_mul_f32 v[118:119], v[198:199], v[118:119] op_sel_hi:[0,1]
	s_waitcnt vmcnt(15)
	v_mul_f32_e32 v6, v117, v133
	v_mul_f32_e32 v7, v119, v135
	v_fmac_f32_e32 v6, v116, v132
	v_fmac_f32_e32 v7, v118, v134
	s_and_b32 s13, s2, 15
	s_mul_i32 s14, s13, 0x104
	s_mul_i32 s15, s13, 0x110
	v_add_f32_e32 v6, v6, v7
	v_add_u32_e32 v125, s14, v59
	ds_write_b32 v125, v6
	v_cvt_pk_bf16_f32 v8, v132, v133
	v_cvt_pk_bf16_f32 v9, v134, v135
	v_add_u32_e32 v10, s15, v76
	s_mov_b64 exec, s[48:49]
	ds_write_b64 v10, v[8:9]
	s_mov_b64 exec, -1
	s_waitcnt vmcnt(14)
	v_mul_f32_e32 v11, v117, v137
	v_mul_f32_e32 v15, v119, v139
	v_fmac_f32_e32 v11, v116, v136
	v_fmac_f32_e32 v15, v118, v138
	s_add_i32 s13, s2, 1
	s_and_b32 s13, s13, 15
	s_mul_i32 s14, s13, 0x104
	s_mul_i32 s15, s13, 0x110
	v_add_f32_e32 v11, v11, v15
	v_add_u32_e32 v16, s14, v59
	ds_write_b32 v16, v11
	v_cvt_pk_bf16_f32 v12, v136, v137
	v_cvt_pk_bf16_f32 v13, v138, v139
	v_add_u32_e32 v14, s15, v76
	s_mov_b64 exec, s[48:49]
	ds_write_b64 v14, v[12:13]
	s_mov_b64 exec, -1
	s_waitcnt vmcnt(13)
	v_mul_f32_e32 v6, v117, v141
	v_mul_f32_e32 v7, v119, v143
	v_fmac_f32_e32 v6, v116, v140
	v_fmac_f32_e32 v7, v118, v142
	s_add_i32 s13, s2, 2
	s_and_b32 s13, s13, 15
	s_mul_i32 s14, s13, 0x104
	s_mul_i32 s15, s13, 0x110
	v_add_f32_e32 v6, v6, v7
	v_add_u32_e32 v125, s14, v59
	ds_write_b32 v125, v6
	v_cvt_pk_bf16_f32 v8, v140, v141
	v_cvt_pk_bf16_f32 v9, v142, v143
	v_add_u32_e32 v10, s15, v76
	s_mov_b64 exec, s[48:49]
	ds_write_b64 v10, v[8:9]
	s_mov_b64 exec, -1
	s_waitcnt vmcnt(12)
	v_mul_f32_e32 v11, v117, v145
	v_mul_f32_e32 v15, v119, v147
	v_fmac_f32_e32 v11, v116, v144
	v_fmac_f32_e32 v15, v118, v146
	s_add_i32 s13, s2, 3
	s_and_b32 s13, s13, 15
	s_mul_i32 s14, s13, 0x104
	s_mul_i32 s15, s13, 0x110
	v_add_f32_e32 v11, v11, v15
	v_add_u32_e32 v16, s14, v59
	ds_write_b32 v16, v11
	v_cvt_pk_bf16_f32 v12, v144, v145
	v_cvt_pk_bf16_f32 v13, v146, v147
	v_add_u32_e32 v14, s15, v76
	s_mov_b64 exec, s[48:49]
	ds_write_b64 v14, v[12:13]
	s_mov_b64 exec, -1
	s_waitcnt vmcnt(11)
	v_mul_f32_e32 v6, v117, v149
	v_mul_f32_e32 v7, v119, v151
	v_fmac_f32_e32 v6, v116, v148
	v_fmac_f32_e32 v7, v118, v150
	s_add_i32 s13, s2, 4
	s_and_b32 s13, s13, 15
	s_mul_i32 s14, s13, 0x104
	s_mul_i32 s15, s13, 0x110
	v_add_f32_e32 v6, v6, v7
	v_add_u32_e32 v125, s14, v59
	ds_write_b32 v125, v6
	v_cvt_pk_bf16_f32 v8, v148, v149
	v_cvt_pk_bf16_f32 v9, v150, v151
	v_add_u32_e32 v10, s15, v76
	s_mov_b64 exec, s[48:49]
	ds_write_b64 v10, v[8:9]
	s_mov_b64 exec, -1
	s_waitcnt vmcnt(10)
	v_mul_f32_e32 v11, v117, v153
	v_mul_f32_e32 v15, v119, v155
	v_fmac_f32_e32 v11, v116, v152
	v_fmac_f32_e32 v15, v118, v154
	s_add_i32 s13, s2, 5
	s_and_b32 s13, s13, 15
	s_mul_i32 s14, s13, 0x104
	s_mul_i32 s15, s13, 0x110
	v_add_f32_e32 v11, v11, v15
	v_add_u32_e32 v16, s14, v59
	ds_write_b32 v16, v11
	v_cvt_pk_bf16_f32 v12, v152, v153
	v_cvt_pk_bf16_f32 v13, v154, v155
	v_add_u32_e32 v14, s15, v76
	s_mov_b64 exec, s[48:49]
	ds_write_b64 v14, v[12:13]
	s_mov_b64 exec, -1
	s_waitcnt vmcnt(9)
	v_mul_f32_e32 v6, v117, v157
	v_mul_f32_e32 v7, v119, v159
	v_fmac_f32_e32 v6, v116, v156
	v_fmac_f32_e32 v7, v118, v158
	s_add_i32 s13, s2, 6
	s_and_b32 s13, s13, 15
	s_mul_i32 s14, s13, 0x104
	s_mul_i32 s15, s13, 0x110
	v_add_f32_e32 v6, v6, v7
	v_add_u32_e32 v125, s14, v59
	ds_write_b32 v125, v6
	v_cvt_pk_bf16_f32 v8, v156, v157
	v_cvt_pk_bf16_f32 v9, v158, v159
	v_add_u32_e32 v10, s15, v76
	s_mov_b64 exec, s[48:49]
	ds_write_b64 v10, v[8:9]
	s_mov_b64 exec, -1
	s_waitcnt vmcnt(8)
	v_mul_f32_e32 v11, v117, v161
	v_mul_f32_e32 v15, v119, v163
	v_fmac_f32_e32 v11, v116, v160
	v_fmac_f32_e32 v15, v118, v162
	s_add_i32 s13, s2, 7
	s_and_b32 s13, s13, 15
	s_mul_i32 s14, s13, 0x104
	s_mul_i32 s15, s13, 0x110
	v_add_f32_e32 v11, v11, v15
	v_add_u32_e32 v16, s14, v59
	ds_write_b32 v16, v11
	v_cvt_pk_bf16_f32 v12, v160, v161
	v_cvt_pk_bf16_f32 v13, v162, v163
	v_add_u32_e32 v14, s15, v76
	s_mov_b64 exec, s[48:49]
	ds_write_b64 v14, v[12:13]
	s_mov_b64 exec, -1
	s_waitcnt vmcnt(7)
	v_mul_f32_e32 v6, v117, v165
	v_mul_f32_e32 v7, v119, v167
	v_fmac_f32_e32 v6, v116, v164
	v_fmac_f32_e32 v7, v118, v166
	s_add_i32 s13, s2, 8
	s_and_b32 s13, s13, 15
	s_mul_i32 s14, s13, 0x104
	s_mul_i32 s15, s13, 0x110
	v_add_f32_e32 v6, v6, v7
	v_add_u32_e32 v125, s14, v59
	ds_write_b32 v125, v6
	v_cvt_pk_bf16_f32 v8, v164, v165
	v_cvt_pk_bf16_f32 v9, v166, v167
	v_add_u32_e32 v10, s15, v76
	s_mov_b64 exec, s[48:49]
	ds_write_b64 v10, v[8:9]
	s_mov_b64 exec, -1
	s_waitcnt vmcnt(6)
	v_mul_f32_e32 v11, v117, v169
	v_mul_f32_e32 v15, v119, v171
	v_fmac_f32_e32 v11, v116, v168
	v_fmac_f32_e32 v15, v118, v170
	s_add_i32 s13, s2, 9
	s_and_b32 s13, s13, 15
	s_mul_i32 s14, s13, 0x104
	s_mul_i32 s15, s13, 0x110
	v_add_f32_e32 v11, v11, v15
	v_add_u32_e32 v16, s14, v59
	ds_write_b32 v16, v11
	v_cvt_pk_bf16_f32 v12, v168, v169
	v_cvt_pk_bf16_f32 v13, v170, v171
	v_add_u32_e32 v14, s15, v76
	s_mov_b64 exec, s[48:49]
	ds_write_b64 v14, v[12:13]
	s_mov_b64 exec, -1
	s_waitcnt vmcnt(5)
	v_mul_f32_e32 v6, v117, v173
	v_mul_f32_e32 v7, v119, v175
	v_fmac_f32_e32 v6, v116, v172
	v_fmac_f32_e32 v7, v118, v174
	s_add_i32 s13, s2, 10
	s_and_b32 s13, s13, 15
	s_mul_i32 s14, s13, 0x104
	s_mul_i32 s15, s13, 0x110
	v_add_f32_e32 v6, v6, v7
	v_add_u32_e32 v125, s14, v59
	ds_write_b32 v125, v6
	v_cvt_pk_bf16_f32 v8, v172, v173
	v_cvt_pk_bf16_f32 v9, v174, v175
	v_add_u32_e32 v10, s15, v76
	s_mov_b64 exec, s[48:49]
	ds_write_b64 v10, v[8:9]
	s_mov_b64 exec, -1
	s_waitcnt vmcnt(4)
	v_mul_f32_e32 v11, v117, v177
	v_mul_f32_e32 v15, v119, v179
	v_fmac_f32_e32 v11, v116, v176
	v_fmac_f32_e32 v15, v118, v178
	s_add_i32 s13, s2, 11
	s_and_b32 s13, s13, 15
	s_mul_i32 s14, s13, 0x104
	s_mul_i32 s15, s13, 0x110
	v_add_f32_e32 v11, v11, v15
	v_add_u32_e32 v16, s14, v59
	ds_write_b32 v16, v11
	v_cvt_pk_bf16_f32 v12, v176, v177
	v_cvt_pk_bf16_f32 v13, v178, v179
	v_add_u32_e32 v14, s15, v76
	s_mov_b64 exec, s[48:49]
	ds_write_b64 v14, v[12:13]
	s_mov_b64 exec, -1
	s_waitcnt vmcnt(3)
	v_mul_f32_e32 v6, v117, v181
	v_mul_f32_e32 v7, v119, v183
	v_fmac_f32_e32 v6, v116, v180
	v_fmac_f32_e32 v7, v118, v182
	s_add_i32 s13, s2, 12
	s_and_b32 s13, s13, 15
	s_mul_i32 s14, s13, 0x104
	s_mul_i32 s15, s13, 0x110
	v_add_f32_e32 v6, v6, v7
	v_add_u32_e32 v125, s14, v59
	ds_write_b32 v125, v6
	v_cvt_pk_bf16_f32 v8, v180, v181
	v_cvt_pk_bf16_f32 v9, v182, v183
	v_add_u32_e32 v10, s15, v76
	s_mov_b64 exec, s[48:49]
	ds_write_b64 v10, v[8:9]
	s_mov_b64 exec, -1
	s_waitcnt vmcnt(2)
	v_mul_f32_e32 v11, v117, v185
	v_mul_f32_e32 v15, v119, v187
	v_fmac_f32_e32 v11, v116, v184
	v_fmac_f32_e32 v15, v118, v186
	s_add_i32 s13, s2, 13
	s_and_b32 s13, s13, 15
	s_mul_i32 s14, s13, 0x104
	s_mul_i32 s15, s13, 0x110
	v_add_f32_e32 v11, v11, v15
	v_add_u32_e32 v16, s14, v59
	ds_write_b32 v16, v11
	v_cvt_pk_bf16_f32 v12, v184, v185
	v_cvt_pk_bf16_f32 v13, v186, v187
	v_add_u32_e32 v14, s15, v76
	s_mov_b64 exec, s[48:49]
	ds_write_b64 v14, v[12:13]
	s_mov_b64 exec, -1
	s_waitcnt vmcnt(1)
	v_mul_f32_e32 v6, v117, v189
	v_mul_f32_e32 v7, v119, v191
	v_fmac_f32_e32 v6, v116, v188
	v_fmac_f32_e32 v7, v118, v190
	s_add_i32 s13, s2, 14
	s_and_b32 s13, s13, 15
	s_mul_i32 s14, s13, 0x104
	s_mul_i32 s15, s13, 0x110
	v_add_f32_e32 v6, v6, v7
	v_add_u32_e32 v125, s14, v59
	ds_write_b32 v125, v6
	v_cvt_pk_bf16_f32 v8, v188, v189
	v_cvt_pk_bf16_f32 v9, v190, v191
	v_add_u32_e32 v10, s15, v76
	s_mov_b64 exec, s[48:49]
	ds_write_b64 v10, v[8:9]
	s_mov_b64 exec, -1
	s_waitcnt vmcnt(0)
	v_mul_f32_e32 v11, v117, v193
	v_mul_f32_e32 v15, v119, v195
	v_fmac_f32_e32 v11, v116, v192
	v_fmac_f32_e32 v15, v118, v194
	s_add_i32 s13, s2, 15
	s_and_b32 s13, s13, 15
	s_mul_i32 s14, s13, 0x104
	s_mul_i32 s15, s13, 0x110
	v_add_f32_e32 v11, v11, v15
	v_add_u32_e32 v16, s14, v59
	ds_write_b32 v16, v11
	v_cvt_pk_bf16_f32 v12, v192, v193
	v_cvt_pk_bf16_f32 v13, v194, v195
	v_add_u32_e32 v14, s15, v76
	s_mov_b64 exec, s[48:49]
	ds_write_b64 v14, v[12:13]
	s_mov_b64 exec, -1
	s_waitcnt lgkmcnt(0)
	ds_read2_b32 v[60:61], v77 offset0:0 offset1:1
	ds_read2_b32 v[62:63], v77 offset0:2 offset1:3
	ds_read2_b32 v[64:65], v77 offset0:4 offset1:5
	ds_read2_b32 v[66:67], v77 offset0:6 offset1:7
	ds_read2_b32 v[68:69], v77 offset0:8 offset1:9
	ds_read2_b32 v[70:71], v77 offset0:10 offset1:11
	ds_read2_b32 v[72:73], v77 offset0:12 offset1:13
	ds_read2_b32 v[74:75], v77 offset0:14 offset1:15
	s_waitcnt lgkmcnt(0)
	v_add_f32_e32 v78, 0, v60
	v_add_f32_e32 v78, v78, v61
	v_add_f32_e32 v78, v78, v62
	v_add_f32_e32 v78, v78, v63
	v_add_f32_e32 v78, v78, v64
	v_add_f32_e32 v78, v78, v65
	v_add_f32_e32 v78, v78, v66
	v_add_f32_e32 v78, v78, v67
	v_add_f32_e32 v78, v78, v68
	v_add_f32_e32 v78, v78, v69
	v_add_f32_e32 v78, v78, v70
	v_add_f32_e32 v78, v78, v71
	v_add_f32_e32 v78, v78, v72
	v_add_f32_e32 v78, v78, v73
	v_add_f32_e32 v78, v78, v74
	v_add_f32_e32 v78, v78, v75
	s_nop 1
	v_add_f32_dpp v78, v78, v78 quad_perm:[1,0,3,2] row_mask:0xf bank_mask:0xf bound_ctrl:1
	s_nop 1
	v_add_f32_dpp v78, v78, v78 quad_perm:[2,3,0,1] row_mask:0xf bank_mask:0xf bound_ctrl:1
	v_lshlrev_b32_e32 v79, 4, v1
	ds_bpermute_b32 v78, v79, v78
	s_waitcnt lgkmcnt(0)
	s_barrier
	ds_read_b128 v[28:31], v54
	ds_read_b128 v[60:63], v57
	ds_read_b128 v[32:35], v54 offset:64
	ds_read_b128 v[64:67], v57 offset:64
	ds_read_b128 v[36:39], v54 offset:128
	ds_read_b128 v[68:71], v57 offset:128
	ds_read_b128 v[40:43], v54 offset:192
	ds_read_b128 v[72:75], v57 offset:192
	s_waitcnt lgkmcnt(6)
	v_mfma_f32_16x16x32_bf16 v[18:21], v[28:31], v[60:63], 0
	s_waitcnt lgkmcnt(4)
	v_mfma_f32_16x16x32_bf16 v[18:21], v[32:35], v[64:67], v[18:21]
	s_waitcnt lgkmcnt(2)
	v_mfma_f32_16x16x32_bf16 v[18:21], v[36:39], v[68:71], v[18:21]
	s_waitcnt lgkmcnt(0)
	v_mfma_f32_16x16x32_bf16 v[18:21], v[40:43], v[72:75], v[18:21]
	s_nop 2
	v_mov_b32_e32 v28, v78
	s_load_dwordx2 s[4:5], s[0:1], 0x70
	v_lshl_or_b32 v30, v24, 2, s3
	v_ashrrev_i32_e32 v31, 31, v30
	v_mov_b32_e32 v107, 0
	s_waitcnt lgkmcnt(0)
	v_add_f32_e32 v34, v130, v28
	v_add_f32_e32 v35, v34, v18
	v_add_f32_e32 v28, v35, v35
	v_mul_f32_e32 v28, 0x3fb8aa3b, v28
	v_exp_f32_e32 v32, v28
	v_lshlrev_b64 v[28:29], 9, v[30:31]
	s_mov_b32 s8, 0x19200
	v_add3_u32 v37, v27, v25, s8
	v_add_f32_e32 v31, 1.0, v32
	v_rcp_f32_e32 v31, v31
	v_lshl_add_u64 v[32:33], s[4:5], 0, v[106:107]
	v_lshl_add_u64 v[28:29], v[32:33], 0, v[28:29]
	global_store_dword v[28:29], v35, off sc1
	v_fma_f32 v35, v31, -2.0, 1.0
	v_fma_f32 v28, -v35, v35, 1.0
	v_mul_f32_e32 v28, v129, v28
	v_add_f32_e32 v31, v34, v19
	v_cvt_pk_bf16_f32 v29, v28, s0
	v_mul_f32_e64 v27, v35, -v28
	v_add_f32_e32 v28, v31, v31
	v_mul_f32_e32 v28, 0x3fb8aa3b, v28
	v_exp_f32_e32 v38, v28
	v_cvt_pk_bf16_f32 v27, v27, s0
	ds_write_b16 v37, v27 offset:4352
	v_or_b32_e32 v28, 1, v30
	v_add_f32_e32 v27, 1.0, v38
	v_rcp_f32_e32 v27, v27
	ds_write_b16 v37, v29
	v_ashrrev_i32_e32 v29, 31, v28
	v_lshlrev_b64 v[28:29], 9, v[28:29]
	v_lshl_add_u64 v[28:29], v[32:33], 0, v[28:29]
	v_fma_f32 v27, v27, -2.0, 1.0
	global_store_dword v[28:29], v31, off sc1
	v_fma_f32 v28, -v27, v27, 1.0
	v_mul_f32_e32 v28, v129, v28
	v_cvt_pk_bf16_f32 v29, v28, s0
	v_add_f32_e32 v31, v34, v20
	ds_write_b16 v37, v29 offset:272
	v_add_f32_e32 v29, v31, v31
	v_mul_f32_e32 v29, 0x3fb8aa3b, v29
	v_exp_f32_e32 v38, v29
	v_mul_f32_e64 v28, v27, -v28
	v_cvt_pk_bf16_f32 v28, v28, s0
	ds_write_b16 v37, v28 offset:4624
	v_add_f32_e32 v38, 1.0, v38
	v_or_b32_e32 v28, 2, v30
	v_rcp_f32_e32 v38, v38
	v_ashrrev_i32_e32 v29, 31, v28
	v_lshlrev_b64 v[28:29], 9, v[28:29]
	v_lshl_add_u64 v[28:29], v[32:33], 0, v[28:29]
	global_store_dword v[28:29], v31, off sc1
	v_fma_f32 v28, v38, -2.0, 1.0
	v_fma_f32 v29, -v28, v28, 1.0
	v_mul_f32_e32 v29, v129, v29
	v_cvt_pk_bf16_f32 v31, v29, s0
	v_add_f32_e32 v34, v34, v21
	ds_write_b16 v37, v31 offset:544
	v_add_f32_e32 v31, v34, v34
	v_mul_f32_e32 v31, 0x3fb8aa3b, v31
	v_exp_f32_e32 v38, v31
	v_mul_f32_e64 v29, v28, -v29
	v_cvt_pk_bf16_f32 v29, v29, s0
	ds_write_b16 v37, v29 offset:4896
	v_add_f32_e32 v29, 1.0, v38
	v_rcp_f32_e32 v29, v29
	v_or_b32_e32 v30, 3, v30
	v_ashrrev_i32_e32 v31, 31, v30
	v_lshlrev_b64 v[30:31], 9, v[30:31]
	v_lshl_add_u64 v[30:31], v[32:33], 0, v[30:31]
	v_fma_f32 v29, v29, -2.0, 1.0
	global_store_dword v[30:31], v34, off sc1
	v_fma_f32 v30, -v29, v29, 1.0
	v_mul_f32_e32 v30, v129, v30
	v_cvt_pk_bf16_f32 v31, v30, s0
	v_mul_f32_e64 v30, v29, -v30
	v_cvt_pk_bf16_f32 v30, v30, s0
	ds_write_b16 v37, v30 offset:5168
	v_mov_b32_e32 v30, 0x1d800
	v_mul_f32_e32 v36, v129, v35
	v_lshl_or_b32 v32, v128, 6, v30
	v_mov_b32_e32 v30, v107
	ds_write_b16 v37, v31 offset:816
	v_mov_b32_e32 v31, 0
	v_mov_b32_dpp v30, v36 quad_perm:[1,0,3,2] row_mask:0xf bank_mask:0xf
	v_fmac_f32_e32 v30, v129, v35
	v_cmp_eq_u32_e32 vcc, 0, v1
	v_add_u32_e32 v26, v32, v26
	v_add_f32_dpp v30, v30, v30 quad_perm:[2,3,0,1] row_mask:0xf bank_mask:0xf bound_ctrl:1
	s_nop 1
	v_add_f32_dpp v30, v30, v30 row_half_mirror row_mask:0xf bank_mask:0xf bound_ctrl:1
	s_nop 1
	v_mov_b32_dpp v31, v30 row_mirror row_mask:0xf bank_mask:0xf
	s_and_saveexec_b64 s[4:5], vcc
	v_add_f32_e32 v30, v30, v31
	ds_write_b32 v26, v30
	s_or_b64 exec, exec, s[4:5]
	v_mul_f32_e32 v30, v129, v27
	v_mov_b32_e32 v31, 0
	s_nop 1
	v_mov_b32_dpp v31, v30 quad_perm:[1,0,3,2] row_mask:0xf bank_mask:0xf
	v_fmac_f32_e32 v31, v129, v27
	s_nop 1
	v_add_f32_dpp v27, v31, v31 quad_perm:[2,3,0,1] row_mask:0xf bank_mask:0xf bound_ctrl:1
	s_nop 1
	v_add_f32_dpp v27, v27, v27 row_half_mirror row_mask:0xf bank_mask:0xf bound_ctrl:1
	s_nop 1
	v_mov_b32_dpp v107, v27 row_mirror row_mask:0xf bank_mask:0xf
	s_and_saveexec_b64 s[4:5], vcc
	v_add_f32_e32 v27, v27, v107
	ds_write_b32 v26, v27 offset:4
	s_or_b64 exec, exec, s[4:5]
	v_mul_f32_e32 v30, v129, v28
	v_mov_b32_e32 v31, 0
	v_mov_b32_e32 v27, 0
	s_nop 0
	v_mov_b32_dpp v31, v30 quad_perm:[1,0,3,2] row_mask:0xf bank_mask:0xf
	v_fmac_f32_e32 v31, v129, v28
	v_mov_b32_e32 v30, 0
	s_nop 0
	v_add_f32_dpp v28, v31, v31 quad_perm:[2,3,0,1] row_mask:0xf bank_mask:0xf bound_ctrl:1
	s_nop 1
	v_add_f32_dpp v28, v28, v28 row_half_mirror row_mask:0xf bank_mask:0xf bound_ctrl:1
	s_nop 1
	v_mov_b32_dpp v30, v28 row_mirror row_mask:0xf bank_mask:0xf
	s_and_saveexec_b64 s[4:5], vcc
	v_add_f32_e32 v28, v28, v30
	ds_write_b32 v26, v28 offset:8
	s_or_b64 exec, exec, s[4:5]
	v_mul_f32_e32 v28, v129, v29
	v_mov_b32_e32 v30, 0
	s_nop 1
	v_mov_b32_dpp v30, v28 quad_perm:[1,0,3,2] row_mask:0xf bank_mask:0xf
	v_fmac_f32_e32 v30, v129, v29
	s_nop 1
	v_add_f32_dpp v28, v30, v30 quad_perm:[2,3,0,1] row_mask:0xf bank_mask:0xf bound_ctrl:1
	s_nop 1
	v_add_f32_dpp v28, v28, v28 row_half_mirror row_mask:0xf bank_mask:0xf bound_ctrl:1
	s_nop 1
	v_mov_b32_dpp v27, v28 row_mirror row_mask:0xf bank_mask:0xf
	s_and_saveexec_b64 s[4:5], vcc
	v_add_f32_e32 v27, v28, v27
	ds_write_b32 v26, v27 offset:12
	s_or_b64 exec, exec, s[4:5]
	s_mov_b64 s[4:5], 0
	s_branch .LBB0_28
.Lp_q:
	s_and_b32 s13, s2, 7
	s_lshl_b32 s14, s13, 13
	v_add_u32_e32 v125, s14, v120
	global_load_dwordx4 v[80:83], v125, s[40:41]
	s_add_i32 s13, s2, 1
	s_and_b32 s13, s13, 7
	s_lshl_b32 s14, s13, 13
	v_add_u32_e32 v125, s14, v120
	global_load_dwordx4 v[84:87], v125, s[40:41]
	s_add_i32 s13, s2, 2
	s_and_b32 s13, s13, 7
	s_lshl_b32 s14, s13, 13
	v_add_u32_e32 v125, s14, v120
	global_load_dwordx4 v[88:91], v125, s[40:41]
	s_add_i32 s13, s2, 3
	s_and_b32 s13, s13, 7
	s_lshl_b32 s14, s13, 13
	v_add_u32_e32 v125, s14, v120
	global_load_dwordx4 v[92:95], v125, s[40:41]
	s_add_i32 s13, s2, 4
	s_and_b32 s13, s13, 7
	s_lshl_b32 s14, s13, 13
	v_add_u32_e32 v125, s14, v120
	global_load_dwordx4 v[96:99], v125, s[40:41]
	s_add_i32 s13, s2, 5
	s_and_b32 s13, s13, 7
	s_lshl_b32 s14, s13, 13
	v_add_u32_e32 v125, s14, v120
	global_load_dwordx4 v[100:103], v125, s[40:41]
	s_add_i32 s13, s2, 6
	s_and_b32 s13, s13, 7
	s_lshl_b32 s14, s13, 13
	v_add_u32_e32 v125, s14, v120
	global_load_dwordx4 v[108:111], v125, s[40:41]
	s_add_i32 s13, s2, 7
	s_and_b32 s13, s13, 7
	s_lshl_b32 s14, s13, 13
	v_add_u32_e32 v125, s14, v120
	global_load_dwordx4 v[112:115], v125, s[40:41]
	global_load_dword v129, v106, s[32:33]
	global_load_dword v130, v106, s[30:31]
	v_lshrrev_b32_e32 v122, 5, v0
	v_lshlrev_b32_e32 v122, 10, v122
	v_and_b32_e32 v125, 31, v0
	v_lshl_add_u32 v122, v125, 4, v122
	s_and_b32 s13, s2, 7
	s_lshl_b32 s14, s13, 14
	v_add_u32_e32 v125, s14, v122
	global_load_dwordx4 v[132:135], v125, s[28:29]
	s_add_i32 s13, s2, 1
	s_and_b32 s13, s13, 7
	s_lshl_b32 s14, s13, 14
	v_add_u32_e32 v125, s14, v122
	global_load_dwordx4 v[136:139], v125, s[28:29]
	s_add_i32 s13, s2, 2
	s_and_b32 s13, s13, 7
	s_lshl_b32 s14, s13, 14
	v_add_u32_e32 v125, s14, v122
	global_load_dwordx4 v[140:143], v125, s[28:29]
	s_add_i32 s13, s2, 3
	s_and_b32 s13, s13, 7
	s_lshl_b32 s14, s13, 14
	v_add_u32_e32 v125, s14, v122
	global_load_dwordx4 v[144:147], v125, s[28:29]
	s_add_i32 s13, s2, 4
	s_and_b32 s13, s13, 7
	s_lshl_b32 s14, s13, 14
	v_add_u32_e32 v125, s14, v122
	global_load_dwordx4 v[148:151], v125, s[28:29]
	s_add_i32 s13, s2, 5
	s_and_b32 s13, s13, 7
	s_lshl_b32 s14, s13, 14
	v_add_u32_e32 v125, s14, v122
	global_load_dwordx4 v[152:155], v125, s[28:29]
	s_add_i32 s13, s2, 6
	s_and_b32 s13, s13, 7
	s_lshl_b32 s14, s13, 14
	v_add_u32_e32 v125, s14, v122
	global_load_dwordx4 v[156:159], v125, s[28:29]
	s_add_i32 s13, s2, 7
	s_and_b32 s13, s13, 7
	s_lshl_b32 s14, s13, 14
	v_add_u32_e32 v125, s14, v122
	global_load_dwordx4 v[160:163], v125, s[28:29]
	s_waitcnt vmcnt(18)
	v_cvt_pk_bf16_f32 v12, v2, v3
	v_cvt_pk_bf16_f32 v13, v4, v5
	ds_write_b64 v124, v[12:13]
	s_waitcnt vmcnt(17)
	v_cvt_pk_bf16_f32 v6, v80, v81
	v_cvt_pk_bf16_f32 v7, v82, v83
	s_and_b32 s13, s2, 7
	s_mul_i32 s14, s13, 0x1100
	v_add_u32_e32 v125, s14, v58
	ds_write_b64 v125, v[6:7]
	s_waitcnt vmcnt(16)
	v_cvt_pk_bf16_f32 v8, v84, v85
	v_cvt_pk_bf16_f32 v9, v86, v87
	s_add_i32 s13, s2, 1
	s_and_b32 s13, s13, 7
	s_mul_i32 s14, s13, 0x1100
	v_add_u32_e32 v10, s14, v58
	ds_write_b64 v10, v[8:9]
	s_waitcnt vmcnt(15)
	v_cvt_pk_bf16_f32 v6, v88, v89
	v_cvt_pk_bf16_f32 v7, v90, v91
	s_add_i32 s13, s2, 2
	s_and_b32 s13, s13, 7
	s_mul_i32 s14, s13, 0x1100
	v_add_u32_e32 v125, s14, v58
	ds_write_b64 v125, v[6:7]
	s_waitcnt vmcnt(14)
	v_cvt_pk_bf16_f32 v8, v92, v93
	v_cvt_pk_bf16_f32 v9, v94, v95
	s_add_i32 s13, s2, 3
	s_and_b32 s13, s13, 7
	s_mul_i32 s14, s13, 0x1100
	v_add_u32_e32 v10, s14, v58
	ds_write_b64 v10, v[8:9]
	s_waitcnt vmcnt(13)
	v_cvt_pk_bf16_f32 v6, v96, v97
	v_cvt_pk_bf16_f32 v7, v98, v99
	s_add_i32 s13, s2, 4
	s_and_b32 s13, s13, 7
	s_mul_i32 s14, s13, 0x1100
	v_add_u32_e32 v125, s14, v58
	ds_write_b64 v125, v[6:7]
	s_waitcnt vmcnt(12)
	v_cvt_pk_bf16_f32 v8, v100, v101
	v_cvt_pk_bf16_f32 v9, v102, v103
	s_add_i32 s13, s2, 5
	s_and_b32 s13, s13, 7
	s_mul_i32 s14, s13, 0x1100
	v_add_u32_e32 v10, s14, v58
	ds_write_b64 v10, v[8:9]
	s_waitcnt vmcnt(11)
	v_cvt_pk_bf16_f32 v6, v108, v109
	v_cvt_pk_bf16_f32 v7, v110, v111
	s_add_i32 s13, s2, 6
	s_and_b32 s13, s13, 7
	s_mul_i32 s14, s13, 0x1100
	v_add_u32_e32 v125, s14, v58
	ds_write_b64 v125, v[6:7]
	s_waitcnt vmcnt(10)
	v_cvt_pk_bf16_f32 v8, v112, v113
	v_cvt_pk_bf16_f32 v9, v114, v115
	s_add_i32 s13, s2, 7
	s_and_b32 s13, s13, 7
	s_mul_i32 s14, s13, 0x1100
	v_add_u32_e32 v10, s14, v58
	ds_write_b64 v10, v[8:9]
	s_waitcnt vmcnt(7)
	v_cvt_pk_bf16_f32 v6, v132, v133
	v_cvt_pk_bf16_f32 v7, v134, v135
	s_and_b32 s13, s2, 7
	s_mul_i32 s14, s13, 0x1100
	s_add_i32 s14, s14, 34816
	v_add_u32_e32 v125, s14, v58
	ds_write_b64 v125, v[6:7]
	s_waitcnt vmcnt(6)
	v_cvt_pk_bf16_f32 v8, v136, v137
	v_cvt_pk_bf16_f32 v9, v138, v139
	s_add_i32 s13, s2, 1
	s_and_b32 s13, s13, 7
	s_mul_i32 s14, s13, 0x1100
	s_add_i32 s14, s14, 34816
	v_add_u32_e32 v10, s14, v58
	ds_write_b64 v10, v[8:9]
	s_waitcnt vmcnt(5)
	v_cvt_pk_bf16_f32 v6, v140, v141
	v_cvt_pk_bf16_f32 v7, v142, v143
	s_add_i32 s13, s2, 2
	s_and_b32 s13, s13, 7
	s_mul_i32 s14, s13, 0x1100
	s_add_i32 s14, s14, 34816
	v_add_u32_e32 v125, s14, v58
	ds_write_b64 v125, v[6:7]
	s_waitcnt vmcnt(4)
	v_cvt_pk_bf16_f32 v8, v144, v145
	v_cvt_pk_bf16_f32 v9, v146, v147
	s_add_i32 s13, s2, 3
	s_and_b32 s13, s13, 7
	s_mul_i32 s14, s13, 0x1100
	s_add_i32 s14, s14, 34816
	v_add_u32_e32 v10, s14, v58
	ds_write_b64 v10, v[8:9]
	s_waitcnt vmcnt(3)
	v_cvt_pk_bf16_f32 v6, v148, v149
	v_cvt_pk_bf16_f32 v7, v150, v151
	s_add_i32 s13, s2, 4
	s_and_b32 s13, s13, 7
	s_mul_i32 s14, s13, 0x1100
	s_add_i32 s14, s14, 34816
	v_add_u32_e32 v125, s14, v58
	ds_write_b64 v125, v[6:7]
	s_waitcnt vmcnt(2)
	v_cvt_pk_bf16_f32 v8, v152, v153
	v_cvt_pk_bf16_f32 v9, v154, v155
	s_add_i32 s13, s2, 5
	s_and_b32 s13, s13, 7
	s_mul_i32 s14, s13, 0x1100
	s_add_i32 s14, s14, 34816
	v_add_u32_e32 v10, s14, v58
	ds_write_b64 v10, v[8:9]
	s_waitcnt vmcnt(1)
	v_cvt_pk_bf16_f32 v6, v156, v157
	v_cvt_pk_bf16_f32 v7, v158, v159
	s_add_i32 s13, s2, 6
	s_and_b32 s13, s13, 7
	s_mul_i32 s14, s13, 0x1100
	s_add_i32 s14, s14, 34816
	v_add_u32_e32 v125, s14, v58
	ds_write_b64 v125, v[6:7]
	s_waitcnt vmcnt(0)
	v_cvt_pk_bf16_f32 v8, v160, v161
	v_cvt_pk_bf16_f32 v9, v162, v163
	s_add_i32 s13, s2, 7
	s_and_b32 s13, s13, 7
	s_mul_i32 s14, s13, 0x1100
	s_add_i32 s14, s14, 34816
	v_add_u32_e32 v10, s14, v58
	ds_write_b64 v10, v[8:9]
	v_lshl_add_u32 v123, v128, 1, s12
	v_lshlrev_b32_e32 v123, 12, v123
	v_lshl_add_u32 v123, v126, 4, v123
	v_add_u32_e32 v125, 0x1000, v123
	global_load_dwordx4 v[2:5], v123, s[34:35] nt
	global_load_dwordx4 v[6:9], v123, s[34:35] offset:1024 nt
	global_load_dwordx4 v[10:13], v123, s[34:35] offset:2048 nt
	global_load_dwordx4 v[14:17], v123, s[34:35] offset:3072 nt
	global_load_dwordx4 v[132:135], v125, s[34:35] nt
	global_load_dwordx4 v[136:139], v125, s[34:35] offset:1024 nt
	global_load_dwordx4 v[140:143], v125, s[34:35] offset:2048 nt
	global_load_dwordx4 v[144:147], v125, s[34:35] offset:3072 nt
	s_waitcnt lgkmcnt(0)
	s_barrier
	ds_read_b128 v[28:31], v53
	ds_read_b128 v[60:63], v56
	ds_read_b128 v[32:35], v53 offset:64
	ds_read_b128 v[64:67], v56 offset:64
	ds_read_b128 v[36:39], v53 offset:128
	ds_read_b128 v[68:71], v56 offset:128
	ds_read_b128 v[40:43], v53 offset:192
	ds_read_b128 v[72:75], v56 offset:192
	s_waitcnt lgkmcnt(6)
	v_mfma_f32_16x16x32_bf16 v[18:21], v[28:31], v[60:63], 0
	s_waitcnt lgkmcnt(4)
	v_mfma_f32_16x16x32_bf16 v[18:21], v[32:35], v[64:67], v[18:21]
	s_waitcnt lgkmcnt(2)
	v_mfma_f32_16x16x32_bf16 v[18:21], v[36:39], v[68:71], v[18:21]
	s_waitcnt lgkmcnt(0)
	v_mfma_f32_16x16x32_bf16 v[18:21], v[40:43], v[72:75], v[18:21]
	s_nop 7
	v_mul_f32_e32 v18, s44, v18
	v_mul_f32_e32 v19, s44, v19
	v_mul_f32_e32 v20, s44, v20
	v_mul_f32_e32 v21, s44, v21
	v_cvt_pk_bf16_f32 v18, v18, v18
	v_cvt_pk_bf16_f32 v19, v19, v19
	v_cvt_pk_bf16_f32 v20, v20, v20
	v_cvt_pk_bf16_f32 v21, v21, v21
	ds_write_b16 v55, v18
	ds_write_b16 v55, v19 offset:272
	ds_write_b16 v55, v20 offset:544
	ds_write_b16 v55, v21 offset:816
	s_waitcnt lgkmcnt(0)
	s_barrier
	ds_read_b128 v[28:31], v54
	ds_read_b128 v[60:63], v57
	ds_read_b128 v[32:35], v54 offset:64
	ds_read_b128 v[64:67], v57 offset:64
	ds_read_b128 v[36:39], v54 offset:128
	ds_read_b128 v[68:71], v57 offset:128
	ds_read_b128 v[40:43], v54 offset:192
	ds_read_b128 v[72:75], v57 offset:192
	s_waitcnt lgkmcnt(6)
	v_mfma_f32_16x16x32_bf16 v[18:21], v[28:31], v[60:63], 0
	s_waitcnt lgkmcnt(4)
	v_mfma_f32_16x16x32_bf16 v[18:21], v[32:35], v[64:67], v[18:21]
	s_waitcnt lgkmcnt(2)
	v_mfma_f32_16x16x32_bf16 v[18:21], v[36:39], v[68:71], v[18:21]
	s_waitcnt lgkmcnt(0)
	v_mfma_f32_16x16x32_bf16 v[18:21], v[40:43], v[72:75], v[18:21]
	s_load_dwordx2 s[4:5], s[0:1], 0x68
	v_lshl_or_b32 v26, v24, 2, s12
	v_mov_b32_e32 v107, 0
	v_ashrrev_i32_e32 v27, 31, v26
	v_lshlrev_b64 v[28:29], 9, v[26:27]
	s_waitcnt lgkmcnt(0)
	v_lshl_add_u64 v[30:31], s[4:5], 0, v[106:107]
	v_lshl_add_u64 v[28:29], v[30:31], 0, v[28:29]
	v_mul_u32_u24_e32 v24, 0x440, v24
	s_mov_b32 s4, 0x19200
	global_store_dword v[28:29], v18, off sc1
	v_add3_u32 v28, v24, v25, s4
	v_mul_f32_e32 v24, v18, v18
	v_cvt_pk_bf16_f32 v27, v18, s0
	v_cvt_pk_bf16_f32 v24, v24, s0
	ds_write_b16 v28, v27
	ds_write_b16 v28, v24 offset:4352
	v_max3_f32 v27, |v18|, 0, |v19|
	v_or_b32_e32 v24, 1, v26
	v_cvt_pk_bf16_f32 v18, v19, s0
	v_ashrrev_i32_e32 v25, 31, v24
	ds_write_b16 v28, v18 offset:272
	v_mul_f32_e32 v18, v19, v19
	v_lshlrev_b64 v[24:25], 9, v[24:25]
	v_cvt_pk_bf16_f32 v18, v18, s0
	v_lshl_add_u64 v[24:25], v[30:31], 0, v[24:25]
	ds_write_b16 v28, v18 offset:4624
	v_or_b32_e32 v18, 2, v26
	global_store_dword v[24:25], v19, off sc1
	v_ashrrev_i32_e32 v19, 31, v18
	v_lshlrev_b64 v[18:19], 9, v[18:19]
	v_lshl_add_u64 v[18:19], v[30:31], 0, v[18:19]
	global_store_dword v[18:19], v20, off sc1
	v_cvt_pk_bf16_f32 v18, v20, s0
	ds_write_b16 v28, v18 offset:544
	v_mul_f32_e32 v18, v20, v20
	v_cvt_pk_bf16_f32 v18, v18, s0
	ds_write_b16 v28, v18 offset:4896
	v_or_b32_e32 v18, 3, v26
	v_ashrrev_i32_e32 v19, 31, v18
	v_lshlrev_b64 v[18:19], 9, v[18:19]
	v_lshl_add_u64 v[18:19], v[30:31], 0, v[18:19]
	global_store_dword v[18:19], v21, off sc1
	v_cvt_pk_bf16_f32 v18, v21, s0
	ds_write_b16 v28, v18 offset:816
	v_mul_f32_e32 v18, v21, v21
	v_cvt_pk_bf16_f32 v18, v18, s0
	v_max3_f32 v20, v27, |v20|, |v21|
	ds_write_b16 v28, v18 offset:5168
	v_mov_b32_e32 v18, v107
	v_mov_b32_e32 v19, v107
	v_cmp_eq_u32_e32 vcc, 0, v126
	v_mov_b32_dpp v18, v20 quad_perm:[1,0,3,2] row_mask:0xf bank_mask:0xf
	v_max_f32_e32 v18, v18, v18
	v_max_f32_e32 v18, v20, v18
	s_nop 1
	v_mov_b32_dpp v19, v18 quad_perm:[2,3,0,1] row_mask:0xf bank_mask:0xf
	v_max_f32_e32 v19, v19, v19
	v_max_f32_e32 v18, v18, v19
	v_mov_b32_e32 v19, v107
	s_nop 1
	v_mov_b32_dpp v19, v18 row_half_mirror row_mask:0xf bank_mask:0xf
	v_max_f32_e32 v19, v19, v19
	v_max_f32_e32 v18, v18, v19
	v_mov_b32_e32 v19, v107
	s_nop 1
	v_mov_b32_dpp v19, v18 row_mirror row_mask:0xf bank_mask:0xf
	v_max_f32_e32 v19, v19, v19
	v_max_f32_e32 v18, v18, v19
	s_nop 0
	v_readlane_b32 s8, v18, 0
	v_readlane_b32 s9, v18, 16
	v_readlane_b32 s10, v18, 32
	v_readlane_b32 s11, v18, 48
	v_and_b32_e32 v18, 0x7fffffff, v129
	s_nop 1
	v_add_f32_dpp v18, v18, |v129| quad_perm:[1,0,3,2] row_mask:0xf bank_mask:0xf bound_ctrl:1
	s_nop 1
	v_add_f32_dpp v18, v18, v18 quad_perm:[2,3,0,1] row_mask:0xf bank_mask:0xf bound_ctrl:1
	s_nop 1
	v_add_f32_dpp v18, v18, v18 row_half_mirror row_mask:0xf bank_mask:0xf bound_ctrl:1
	s_nop 1
	v_mov_b32_dpp v107, v18 row_mirror row_mask:0xf bank_mask:0xf
	s_and_saveexec_b64 s[4:5], vcc
	s_cbranch_execz .LBB0_27
	v_mov_b32_e32 v19, 0x1d800
	v_lshl_or_b32 v20, v128, 6, v19
	v_add_f32_e32 v19, v18, v107
	v_max_f32_e64 v18, s11, s11
	v_max_f32_e64 v21, s10, s10
	v_max_f32_e32 v18, v21, v18
	v_mov_b32_e32 v21, s9
	v_max3_f32 v18, s8, v21, v18
	ds_write_b64 v20, v[18:19]
